# v3 + per-tile accumulator clear by 64 v_mov_b64 of inline 0 instead of 128 32-bit copies in all 12 GEMM instances
# baseline (speedup 1.0000x reference)
.LBB0_102:
	s_ashr_i32 s29, s28, 31
	s_lshl_b64 s[30:31], s[28:29], 19
	s_add_u32 s30, s74, s30
	s_addc_u32 s31, s75, s31
	s_ashr_i32 s11, s10, 31
	s_lshl_b64 s[34:35], s[10:11], 19
	s_add_u32 s34, s76, s34
	v_mov_b64_e32 v[0:1], 0
	v_mov_b64_e32 v[2:3], 0
	v_mov_b64_e32 v[4:5], 0
	v_mov_b64_e32 v[6:7], 0
	v_mov_b64_e32 v[8:9], 0
	v_mov_b64_e32 v[10:11], 0
	v_mov_b64_e32 v[12:13], 0
	v_mov_b64_e32 v[14:15], 0
	v_mov_b64_e32 v[16:17], 0
	v_mov_b64_e32 v[18:19], 0
	v_mov_b64_e32 v[20:21], 0
	v_mov_b64_e32 v[22:23], 0
	v_mov_b64_e32 v[24:25], 0
	v_mov_b64_e32 v[26:27], 0
	v_mov_b64_e32 v[28:29], 0
	v_mov_b64_e32 v[30:31], 0
	v_mov_b64_e32 v[32:33], 0
	v_mov_b64_e32 v[34:35], 0
	v_mov_b64_e32 v[36:37], 0
	v_mov_b64_e32 v[38:39], 0
	v_mov_b64_e32 v[40:41], 0
	v_mov_b64_e32 v[42:43], 0
	v_mov_b64_e32 v[44:45], 0
	v_mov_b64_e32 v[46:47], 0
	v_mov_b64_e32 v[48:49], 0
	v_mov_b64_e32 v[50:51], 0
	v_mov_b64_e32 v[52:53], 0
	v_mov_b64_e32 v[54:55], 0
	v_mov_b64_e32 v[56:57], 0
	v_mov_b64_e32 v[58:59], 0
	v_mov_b64_e32 v[60:61], 0
	v_mov_b64_e32 v[62:63], 0
	v_mov_b64_e32 v[64:65], 0
	v_mov_b64_e32 v[66:67], 0
	v_mov_b64_e32 v[68:69], 0
	v_mov_b64_e32 v[70:71], 0
	v_mov_b64_e32 v[72:73], 0
	v_mov_b64_e32 v[74:75], 0
	v_mov_b64_e32 v[76:77], 0
	v_mov_b64_e32 v[78:79], 0
	v_mov_b64_e32 v[80:81], 0
	v_mov_b64_e32 v[82:83], 0
	v_mov_b64_e32 v[84:85], 0
	v_mov_b64_e32 v[86:87], 0
	v_mov_b64_e32 v[88:89], 0
	v_mov_b64_e32 v[90:91], 0
	v_mov_b64_e32 v[92:93], 0
	v_mov_b64_e32 v[94:95], 0
	v_mov_b64_e32 v[96:97], 0
	v_mov_b64_e32 v[98:99], 0
	v_mov_b64_e32 v[100:101], 0
	v_mov_b64_e32 v[102:103], 0
	v_mov_b64_e32 v[104:105], 0
	v_mov_b64_e32 v[106:107], 0
	v_mov_b64_e32 v[108:109], 0
	v_mov_b64_e32 v[110:111], 0
	v_mov_b64_e32 v[112:113], 0
	v_mov_b64_e32 v[114:115], 0
	v_mov_b64_e32 v[116:117], 0
	v_mov_b64_e32 v[118:119], 0
	v_mov_b64_e32 v[120:121], 0
	v_mov_b64_e32 v[122:123], 0
	v_mov_b64_e32 v[124:125], 0
	v_mov_b64_e32 v[126:127], 0
	s_addc_u32 s35, s77, s35
	s_mov_b32 s11, 0
	v_lshl_add_u64 v[144:145], s[60:61], 0, v[136:137]
	v_lshl_add_u64 v[146:147], s[60:61], 0, v[138:139]

.LBB0_123:
	s_ashr_i32 s57, s56, 31
	s_lshl_b64 s[36:37], s[56:57], 19
	s_add_u32 s60, s77, s36
	s_addc_u32 s61, s84, s37
	s_ashr_i32 s39, s38, 31
	s_lshl_b64 s[36:37], s[38:39], 19
	s_add_u32 s74, s85, s36
	v_mov_b64_e32 v[0:1], 0
	v_mov_b64_e32 v[2:3], 0
	v_mov_b64_e32 v[4:5], 0
	v_mov_b64_e32 v[6:7], 0
	v_mov_b64_e32 v[8:9], 0
	v_mov_b64_e32 v[10:11], 0
	v_mov_b64_e32 v[12:13], 0
	v_mov_b64_e32 v[14:15], 0
	v_mov_b64_e32 v[16:17], 0
	v_mov_b64_e32 v[18:19], 0
	v_mov_b64_e32 v[20:21], 0
	v_mov_b64_e32 v[22:23], 0
	v_mov_b64_e32 v[24:25], 0
	v_mov_b64_e32 v[26:27], 0
	v_mov_b64_e32 v[28:29], 0
	v_mov_b64_e32 v[30:31], 0
	v_mov_b64_e32 v[32:33], 0
	v_mov_b64_e32 v[34:35], 0
	v_mov_b64_e32 v[36:37], 0
	v_mov_b64_e32 v[38:39], 0
	v_mov_b64_e32 v[40:41], 0
	v_mov_b64_e32 v[42:43], 0
	v_mov_b64_e32 v[44:45], 0
	v_mov_b64_e32 v[46:47], 0
	v_mov_b64_e32 v[48:49], 0
	v_mov_b64_e32 v[50:51], 0
	v_mov_b64_e32 v[52:53], 0
	v_mov_b64_e32 v[54:55], 0
	v_mov_b64_e32 v[56:57], 0
	v_mov_b64_e32 v[58:59], 0
	v_mov_b64_e32 v[60:61], 0
	v_mov_b64_e32 v[62:63], 0
	v_mov_b64_e32 v[64:65], 0
	v_mov_b64_e32 v[66:67], 0
	v_mov_b64_e32 v[68:69], 0
	v_mov_b64_e32 v[70:71], 0
	v_mov_b64_e32 v[72:73], 0
	v_mov_b64_e32 v[74:75], 0
	v_mov_b64_e32 v[76:77], 0
	v_mov_b64_e32 v[78:79], 0
	v_mov_b64_e32 v[80:81], 0
	v_mov_b64_e32 v[82:83], 0
	v_mov_b64_e32 v[84:85], 0
	v_mov_b64_e32 v[86:87], 0
	v_mov_b64_e32 v[88:89], 0
	v_mov_b64_e32 v[90:91], 0
	v_mov_b64_e32 v[92:93], 0
	v_mov_b64_e32 v[94:95], 0
	v_mov_b64_e32 v[96:97], 0
	v_mov_b64_e32 v[98:99], 0
	v_mov_b64_e32 v[100:101], 0
	v_mov_b64_e32 v[102:103], 0
	v_mov_b64_e32 v[104:105], 0
	v_mov_b64_e32 v[106:107], 0
	v_mov_b64_e32 v[108:109], 0
	v_mov_b64_e32 v[110:111], 0
	v_mov_b64_e32 v[112:113], 0
	v_mov_b64_e32 v[114:115], 0
	v_mov_b64_e32 v[116:117], 0
	v_mov_b64_e32 v[118:119], 0
	v_mov_b64_e32 v[120:121], 0
	v_mov_b64_e32 v[122:123], 0
	v_mov_b64_e32 v[124:125], 0
	v_mov_b64_e32 v[126:127], 0
	s_addc_u32 s75, s86, s37
	s_mov_b32 s0, 0
	v_lshl_add_u64 v[128:129], s[80:81], 0, v[144:145]
	v_lshl_add_u64 v[130:131], s[80:81], 0, v[146:147]

.LBB0_516:
	s_ashr_i32 s39, s38, 31
	s_lshl_b64 s[36:37], s[38:39], 19
	s_add_u32 s40, s51, s36
	s_addc_u32 s41, s56, s37
	s_ashr_i32 s35, s34, 31
	s_lshl_b64 s[36:37], s[34:35], 19
	s_add_u32 s42, s57, s36
	v_mov_b64_e32 v[0:1], 0
	v_mov_b64_e32 v[2:3], 0
	v_mov_b64_e32 v[4:5], 0
	v_mov_b64_e32 v[6:7], 0
	v_mov_b64_e32 v[8:9], 0
	v_mov_b64_e32 v[10:11], 0
	v_mov_b64_e32 v[12:13], 0
	v_mov_b64_e32 v[14:15], 0
	v_mov_b64_e32 v[16:17], 0
	v_mov_b64_e32 v[18:19], 0
	v_mov_b64_e32 v[20:21], 0
	v_mov_b64_e32 v[22:23], 0
	v_mov_b64_e32 v[24:25], 0
	v_mov_b64_e32 v[26:27], 0
	v_mov_b64_e32 v[28:29], 0
	v_mov_b64_e32 v[30:31], 0
	v_mov_b64_e32 v[32:33], 0
	v_mov_b64_e32 v[34:35], 0
	v_mov_b64_e32 v[36:37], 0
	v_mov_b64_e32 v[38:39], 0
	v_mov_b64_e32 v[40:41], 0
	v_mov_b64_e32 v[42:43], 0
	v_mov_b64_e32 v[44:45], 0
	v_mov_b64_e32 v[46:47], 0
	v_mov_b64_e32 v[48:49], 0
	v_mov_b64_e32 v[50:51], 0
	v_mov_b64_e32 v[52:53], 0
	v_mov_b64_e32 v[54:55], 0
	v_mov_b64_e32 v[56:57], 0
	v_mov_b64_e32 v[58:59], 0
	v_mov_b64_e32 v[60:61], 0
	v_mov_b64_e32 v[62:63], 0
	v_mov_b64_e32 v[64:65], 0
	v_mov_b64_e32 v[66:67], 0
	v_mov_b64_e32 v[68:69], 0
	v_mov_b64_e32 v[70:71], 0
	v_mov_b64_e32 v[80:81], 0
	v_mov_b64_e32 v[82:83], 0
	v_mov_b64_e32 v[84:85], 0
	v_mov_b64_e32 v[86:87], 0
	v_mov_b64_e32 v[96:97], 0
	v_mov_b64_e32 v[98:99], 0
	v_mov_b64_e32 v[100:101], 0
	v_mov_b64_e32 v[102:103], 0
	v_mov_b64_e32 v[104:105], 0
	v_mov_b64_e32 v[106:107], 0
	v_mov_b64_e32 v[108:109], 0
	v_mov_b64_e32 v[110:111], 0
	v_mov_b64_e32 v[112:113], 0
	v_mov_b64_e32 v[114:115], 0
	v_mov_b64_e32 v[116:117], 0
	v_mov_b64_e32 v[118:119], 0
	v_mov_b64_e32 v[120:121], 0
	v_mov_b64_e32 v[122:123], 0
	v_mov_b64_e32 v[124:125], 0
	v_mov_b64_e32 v[126:127], 0
	v_mov_b64_e32 v[128:129], 0
	v_mov_b64_e32 v[130:131], 0
	v_mov_b64_e32 v[132:133], 0
	v_mov_b64_e32 v[134:135], 0
	v_mov_b64_e32 v[136:137], 0
	v_mov_b64_e32 v[138:139], 0
	v_mov_b64_e32 v[140:141], 0
	v_mov_b64_e32 v[142:143], 0
	s_addc_u32 s43, s58, s37
	v_lshl_add_u64 v[72:73], s[48:49], 0, v[174:175]
	v_lshl_add_u64 v[74:75], s[48:49], 0, v[176:177]
	s_mov_b32 s35, 0
	s_waitcnt lgkmcnt(0)

.LBB0_593:
	s_ashr_i32 s17, s16, 31
	s_lshl_b64 s[22:23], s[16:17], 18
	s_add_u32 s22, s43, s22
	s_addc_u32 s23, s46, s23
	s_ashr_i32 s15, s14, 31
	s_lshl_b64 s[26:27], s[14:15], 18
	s_add_u32 s26, s47, s26
	v_mov_b64_e32 v[32:33], 0
	v_mov_b64_e32 v[34:35], 0
	v_mov_b64_e32 v[36:37], 0
	v_mov_b64_e32 v[38:39], 0
	v_mov_b64_e32 v[40:41], 0
	v_mov_b64_e32 v[42:43], 0
	v_mov_b64_e32 v[44:45], 0
	v_mov_b64_e32 v[46:47], 0
	v_mov_b64_e32 v[48:49], 0
	v_mov_b64_e32 v[50:51], 0
	v_mov_b64_e32 v[52:53], 0
	v_mov_b64_e32 v[54:55], 0
	v_mov_b64_e32 v[56:57], 0
	v_mov_b64_e32 v[58:59], 0
	v_mov_b64_e32 v[60:61], 0
	v_mov_b64_e32 v[62:63], 0
	v_mov_b64_e32 v[64:65], 0
	v_mov_b64_e32 v[66:67], 0
	v_mov_b64_e32 v[68:69], 0
	v_mov_b64_e32 v[70:71], 0
	v_mov_b64_e32 v[72:73], 0
	v_mov_b64_e32 v[74:75], 0
	v_mov_b64_e32 v[76:77], 0
	v_mov_b64_e32 v[78:79], 0
	v_mov_b64_e32 v[80:81], 0
	v_mov_b64_e32 v[82:83], 0
	v_mov_b64_e32 v[84:85], 0
	v_mov_b64_e32 v[86:87], 0
	v_mov_b64_e32 v[88:89], 0
	v_mov_b64_e32 v[90:91], 0
	v_mov_b64_e32 v[92:93], 0
	v_mov_b64_e32 v[94:95], 0
	v_mov_b64_e32 v[96:97], 0
	v_mov_b64_e32 v[98:99], 0
	v_mov_b64_e32 v[100:101], 0
	v_mov_b64_e32 v[102:103], 0
	v_mov_b64_e32 v[104:105], 0
	v_mov_b64_e32 v[106:107], 0
	v_mov_b64_e32 v[108:109], 0
	v_mov_b64_e32 v[110:111], 0
	v_mov_b64_e32 v[112:113], 0
	v_mov_b64_e32 v[114:115], 0
	v_mov_b64_e32 v[116:117], 0
	v_mov_b64_e32 v[118:119], 0
	v_mov_b64_e32 v[120:121], 0
	v_mov_b64_e32 v[122:123], 0
	v_mov_b64_e32 v[124:125], 0
	v_mov_b64_e32 v[126:127], 0
	v_mov_b64_e32 v[128:129], 0
	v_mov_b64_e32 v[130:131], 0
	v_mov_b64_e32 v[132:133], 0
	v_mov_b64_e32 v[134:135], 0
	v_mov_b64_e32 v[136:137], 0
	v_mov_b64_e32 v[138:139], 0
	v_mov_b64_e32 v[140:141], 0
	v_mov_b64_e32 v[142:143], 0
	v_mov_b64_e32 v[144:145], 0
	v_mov_b64_e32 v[146:147], 0
	v_mov_b64_e32 v[148:149], 0
	v_mov_b64_e32 v[150:151], 0
	v_mov_b64_e32 v[152:153], 0
	v_mov_b64_e32 v[154:155], 0
	v_mov_b64_e32 v[156:157], 0
	v_mov_b64_e32 v[158:159], 0
	s_addc_u32 s27, s48, s27
	v_lshl_add_u64 v[178:179], s[34:35], 0, v[170:171]
	v_lshl_add_u64 v[180:181], s[34:35], 0, v[172:173]
	s_mov_b32 s15, 0

.LBB0_672:
	s_mul_i32 s34, s64, 0xb0000
	s_mul_hi_i32 s0, s64, 0xb0000
	s_add_u32 s34, s42, s34
	s_addc_u32 s35, s43, s0
	s_mul_i32 s36, s63, 0xb0000
	s_mul_hi_i32 s0, s63, 0xb0000
	s_add_u32 s38, s46, s36
	v_mov_b64_e32 v[32:33], 0
	v_mov_b64_e32 v[34:35], 0
	v_mov_b64_e32 v[36:37], 0
	v_mov_b64_e32 v[38:39], 0
	v_mov_b64_e32 v[40:41], 0
	v_mov_b64_e32 v[42:43], 0
	v_mov_b64_e32 v[44:45], 0
	v_mov_b64_e32 v[46:47], 0
	v_mov_b64_e32 v[48:49], 0
	v_mov_b64_e32 v[50:51], 0
	v_mov_b64_e32 v[52:53], 0
	v_mov_b64_e32 v[54:55], 0
	v_mov_b64_e32 v[56:57], 0
	v_mov_b64_e32 v[58:59], 0
	v_mov_b64_e32 v[60:61], 0
	v_mov_b64_e32 v[62:63], 0
	v_mov_b64_e32 v[64:65], 0
	v_mov_b64_e32 v[66:67], 0
	v_mov_b64_e32 v[68:69], 0
	v_mov_b64_e32 v[70:71], 0
	v_mov_b64_e32 v[72:73], 0
	v_mov_b64_e32 v[74:75], 0
	v_mov_b64_e32 v[76:77], 0
	v_mov_b64_e32 v[78:79], 0
	v_mov_b64_e32 v[80:81], 0
	v_mov_b64_e32 v[82:83], 0
	v_mov_b64_e32 v[84:85], 0
	v_mov_b64_e32 v[86:87], 0
	v_mov_b64_e32 v[88:89], 0
	v_mov_b64_e32 v[90:91], 0
	v_mov_b64_e32 v[92:93], 0
	v_mov_b64_e32 v[94:95], 0
	v_mov_b64_e32 v[96:97], 0
	v_mov_b64_e32 v[98:99], 0
	v_mov_b64_e32 v[100:101], 0
	v_mov_b64_e32 v[102:103], 0
	v_mov_b64_e32 v[104:105], 0
	v_mov_b64_e32 v[106:107], 0
	v_mov_b64_e32 v[108:109], 0
	v_mov_b64_e32 v[110:111], 0
	v_mov_b64_e32 v[112:113], 0
	v_mov_b64_e32 v[114:115], 0
	v_mov_b64_e32 v[116:117], 0
	v_mov_b64_e32 v[118:119], 0
	v_mov_b64_e32 v[120:121], 0
	v_mov_b64_e32 v[122:123], 0
	v_mov_b64_e32 v[124:125], 0
	v_mov_b64_e32 v[126:127], 0
	v_mov_b64_e32 v[128:129], 0
	v_mov_b64_e32 v[130:131], 0
	v_mov_b64_e32 v[132:133], 0
	v_mov_b64_e32 v[134:135], 0
	v_mov_b64_e32 v[136:137], 0
	v_mov_b64_e32 v[138:139], 0
	v_mov_b64_e32 v[140:141], 0
	v_mov_b64_e32 v[142:143], 0
	v_mov_b64_e32 v[144:145], 0
	v_mov_b64_e32 v[146:147], 0
	v_mov_b64_e32 v[148:149], 0
	v_mov_b64_e32 v[150:151], 0
	v_mov_b64_e32 v[152:153], 0
	v_mov_b64_e32 v[154:155], 0
	v_mov_b64_e32 v[156:157], 0
	v_mov_b64_e32 v[158:159], 0
	s_addc_u32 s39, s47, s0
	v_lshl_add_u64 v[178:179], s[40:41], 0, v[170:171]
	v_lshl_add_u64 v[180:181], s[40:41], 0, v[172:173]
	s_mov_b32 s67, 0

.LBB0_745:
	s_ashr_i32 s17, s16, 31
	s_lshl_b64 s[22:23], s[16:17], 18
	s_add_u32 s22, s40, s22
	s_addc_u32 s23, s41, s23
	s_ashr_i32 s15, s14, 31
	s_lshl_b64 s[26:27], s[14:15], 18
	s_add_u32 s26, s42, s26
	v_mov_b64_e32 v[32:33], 0
	v_mov_b64_e32 v[34:35], 0
	v_mov_b64_e32 v[36:37], 0
	v_mov_b64_e32 v[38:39], 0
	v_mov_b64_e32 v[40:41], 0
	v_mov_b64_e32 v[42:43], 0
	v_mov_b64_e32 v[44:45], 0
	v_mov_b64_e32 v[46:47], 0
	v_mov_b64_e32 v[48:49], 0
	v_mov_b64_e32 v[50:51], 0
	v_mov_b64_e32 v[52:53], 0
	v_mov_b64_e32 v[54:55], 0
	v_mov_b64_e32 v[56:57], 0
	v_mov_b64_e32 v[58:59], 0
	v_mov_b64_e32 v[60:61], 0
	v_mov_b64_e32 v[62:63], 0
	v_mov_b64_e32 v[64:65], 0
	v_mov_b64_e32 v[66:67], 0
	v_mov_b64_e32 v[68:69], 0
	v_mov_b64_e32 v[70:71], 0
	v_mov_b64_e32 v[72:73], 0
	v_mov_b64_e32 v[74:75], 0
	v_mov_b64_e32 v[76:77], 0
	v_mov_b64_e32 v[78:79], 0
	v_mov_b64_e32 v[80:81], 0
	v_mov_b64_e32 v[82:83], 0
	v_mov_b64_e32 v[84:85], 0
	v_mov_b64_e32 v[86:87], 0
	v_mov_b64_e32 v[88:89], 0
	v_mov_b64_e32 v[90:91], 0
	v_mov_b64_e32 v[92:93], 0
	v_mov_b64_e32 v[94:95], 0
	v_mov_b64_e32 v[96:97], 0
	v_mov_b64_e32 v[98:99], 0
	v_mov_b64_e32 v[100:101], 0
	v_mov_b64_e32 v[102:103], 0
	v_mov_b64_e32 v[104:105], 0
	v_mov_b64_e32 v[106:107], 0
	v_mov_b64_e32 v[108:109], 0
	v_mov_b64_e32 v[110:111], 0
	v_mov_b64_e32 v[112:113], 0
	v_mov_b64_e32 v[114:115], 0
	v_mov_b64_e32 v[116:117], 0
	v_mov_b64_e32 v[118:119], 0
	v_mov_b64_e32 v[120:121], 0
	v_mov_b64_e32 v[122:123], 0
	v_mov_b64_e32 v[124:125], 0
	v_mov_b64_e32 v[126:127], 0
	v_mov_b64_e32 v[128:129], 0
	v_mov_b64_e32 v[130:131], 0
	v_mov_b64_e32 v[132:133], 0
	v_mov_b64_e32 v[134:135], 0
	v_mov_b64_e32 v[136:137], 0
	v_mov_b64_e32 v[138:139], 0
	v_mov_b64_e32 v[140:141], 0
	v_mov_b64_e32 v[142:143], 0
	v_mov_b64_e32 v[144:145], 0
	v_mov_b64_e32 v[146:147], 0
	v_mov_b64_e32 v[148:149], 0
	v_mov_b64_e32 v[150:151], 0
	v_mov_b64_e32 v[152:153], 0
	v_mov_b64_e32 v[154:155], 0
	v_mov_b64_e32 v[156:157], 0
	v_mov_b64_e32 v[158:159], 0
	s_addc_u32 s27, s43, s27
	v_lshl_add_u64 v[180:181], s[34:35], 0, v[172:173]
	v_lshl_add_u64 v[182:183], s[34:35], 0, v[174:175]
	s_mov_b32 s15, 0

.LBB0_772:
	s_ashr_i32 s9, s8, 31
	s_lshl_b64 s[18:19], s[8:9], 18
	s_add_u32 s18, s36, s18
	s_addc_u32 s19, s37, s19
	s_ashr_i32 s17, s16, 31
	s_lshl_b64 s[22:23], s[16:17], 18
	s_add_u32 s22, s40, s22
	v_mov_b64_e32 v[32:33], 0
	v_mov_b64_e32 v[34:35], 0
	v_mov_b64_e32 v[36:37], 0
	v_mov_b64_e32 v[38:39], 0
	v_mov_b64_e32 v[40:41], 0
	v_mov_b64_e32 v[42:43], 0
	v_mov_b64_e32 v[44:45], 0
	v_mov_b64_e32 v[46:47], 0
	v_mov_b64_e32 v[48:49], 0
	v_mov_b64_e32 v[50:51], 0
	v_mov_b64_e32 v[52:53], 0
	v_mov_b64_e32 v[54:55], 0
	v_mov_b64_e32 v[56:57], 0
	v_mov_b64_e32 v[58:59], 0
	v_mov_b64_e32 v[60:61], 0
	v_mov_b64_e32 v[62:63], 0
	v_mov_b64_e32 v[64:65], 0
	v_mov_b64_e32 v[66:67], 0
	v_mov_b64_e32 v[68:69], 0
	v_mov_b64_e32 v[70:71], 0
	v_mov_b64_e32 v[72:73], 0
	v_mov_b64_e32 v[74:75], 0
	v_mov_b64_e32 v[76:77], 0
	v_mov_b64_e32 v[78:79], 0
	v_mov_b64_e32 v[80:81], 0
	v_mov_b64_e32 v[82:83], 0
	v_mov_b64_e32 v[84:85], 0
	v_mov_b64_e32 v[86:87], 0
	v_mov_b64_e32 v[88:89], 0
	v_mov_b64_e32 v[90:91], 0
	v_mov_b64_e32 v[92:93], 0
	v_mov_b64_e32 v[94:95], 0
	v_mov_b64_e32 v[96:97], 0
	v_mov_b64_e32 v[98:99], 0
	v_mov_b64_e32 v[100:101], 0
	v_mov_b64_e32 v[102:103], 0
	v_mov_b64_e32 v[104:105], 0
	v_mov_b64_e32 v[106:107], 0
	v_mov_b64_e32 v[108:109], 0
	v_mov_b64_e32 v[110:111], 0
	v_mov_b64_e32 v[112:113], 0
	v_mov_b64_e32 v[114:115], 0
	v_mov_b64_e32 v[116:117], 0
	v_mov_b64_e32 v[118:119], 0
	v_mov_b64_e32 v[120:121], 0
	v_mov_b64_e32 v[122:123], 0
	v_mov_b64_e32 v[124:125], 0
	v_mov_b64_e32 v[126:127], 0
	v_mov_b64_e32 v[128:129], 0
	v_mov_b64_e32 v[130:131], 0
	v_mov_b64_e32 v[132:133], 0
	v_mov_b64_e32 v[134:135], 0
	v_mov_b64_e32 v[136:137], 0
	v_mov_b64_e32 v[138:139], 0
	v_mov_b64_e32 v[140:141], 0
	v_mov_b64_e32 v[142:143], 0
	v_mov_b64_e32 v[144:145], 0
	v_mov_b64_e32 v[146:147], 0
	v_mov_b64_e32 v[148:149], 0
	v_mov_b64_e32 v[150:151], 0
	v_mov_b64_e32 v[152:153], 0
	v_mov_b64_e32 v[154:155], 0
	v_mov_b64_e32 v[156:157], 0
	v_mov_b64_e32 v[158:159], 0
	s_addc_u32 s23, s41, s23
	v_lshl_add_u64 v[194:195], s[28:29], 0, v[186:187]
	v_lshl_add_u64 v[196:197], s[28:29], 0, v[188:189]
	s_mov_b32 s9, 0

.LBB0_958:
	s_ashr_i32 s23, s22, 31
	s_lshl_b64 s[30:31], s[22:23], 18
	s_add_u32 s30, s42, s30
	s_addc_u32 s31, s43, s31
	s_ashr_i32 s21, s20, 31
	s_lshl_b64 s[34:35], s[20:21], 18
	s_add_u32 s34, s46, s34
	v_mov_b64_e32 v[32:33], 0
	v_mov_b64_e32 v[34:35], 0
	v_mov_b64_e32 v[36:37], 0
	v_mov_b64_e32 v[38:39], 0
	v_mov_b64_e32 v[40:41], 0
	v_mov_b64_e32 v[42:43], 0
	v_mov_b64_e32 v[44:45], 0
	v_mov_b64_e32 v[46:47], 0
	v_mov_b64_e32 v[48:49], 0
	v_mov_b64_e32 v[50:51], 0
	v_mov_b64_e32 v[52:53], 0
	v_mov_b64_e32 v[54:55], 0
	v_mov_b64_e32 v[56:57], 0
	v_mov_b64_e32 v[58:59], 0
	v_mov_b64_e32 v[60:61], 0
	v_mov_b64_e32 v[62:63], 0
	v_mov_b64_e32 v[64:65], 0
	v_mov_b64_e32 v[66:67], 0
	v_mov_b64_e32 v[68:69], 0
	v_mov_b64_e32 v[70:71], 0
	v_mov_b64_e32 v[72:73], 0
	v_mov_b64_e32 v[74:75], 0
	v_mov_b64_e32 v[76:77], 0
	v_mov_b64_e32 v[78:79], 0
	v_mov_b64_e32 v[80:81], 0
	v_mov_b64_e32 v[82:83], 0
	v_mov_b64_e32 v[84:85], 0
	v_mov_b64_e32 v[86:87], 0
	v_mov_b64_e32 v[88:89], 0
	v_mov_b64_e32 v[90:91], 0
	v_mov_b64_e32 v[92:93], 0
	v_mov_b64_e32 v[94:95], 0
	v_mov_b64_e32 v[96:97], 0
	v_mov_b64_e32 v[98:99], 0
	v_mov_b64_e32 v[100:101], 0
	v_mov_b64_e32 v[102:103], 0
	v_mov_b64_e32 v[104:105], 0
	v_mov_b64_e32 v[106:107], 0
	v_mov_b64_e32 v[108:109], 0
	v_mov_b64_e32 v[110:111], 0
	v_mov_b64_e32 v[112:113], 0
	v_mov_b64_e32 v[114:115], 0
	v_mov_b64_e32 v[116:117], 0
	v_mov_b64_e32 v[118:119], 0
	v_mov_b64_e32 v[120:121], 0
	v_mov_b64_e32 v[122:123], 0
	v_mov_b64_e32 v[124:125], 0
	v_mov_b64_e32 v[126:127], 0
	v_mov_b64_e32 v[128:129], 0
	v_mov_b64_e32 v[130:131], 0
	v_mov_b64_e32 v[132:133], 0
	v_mov_b64_e32 v[134:135], 0
	v_mov_b64_e32 v[136:137], 0
	v_mov_b64_e32 v[138:139], 0
	v_mov_b64_e32 v[140:141], 0
	v_mov_b64_e32 v[142:143], 0
	v_mov_b64_e32 v[144:145], 0
	v_mov_b64_e32 v[146:147], 0
	v_mov_b64_e32 v[148:149], 0
	v_mov_b64_e32 v[150:151], 0
	v_mov_b64_e32 v[152:153], 0
	v_mov_b64_e32 v[154:155], 0
	v_mov_b64_e32 v[156:157], 0
	v_mov_b64_e32 v[158:159], 0
	s_addc_u32 s35, s47, s35
	v_lshl_add_u64 v[178:179], s[40:41], 0, v[170:171]
	v_lshl_add_u64 v[180:181], s[40:41], 0, v[172:173]
	s_mov_b32 s21, 0

.LBB0_1181:
	v_mul_hi_u32 v1, v221, s6
	v_mul_lo_u32 v0, v221, s6
	s_ashr_i32 s25, s24, 31
	v_lshl_add_u64 v[0:1], s[10:11], 0, v[0:1]
	s_lshl_b64 s[30:31], s[24:25], 18
	v_mov_b64_e32 v[64:65], 0
	v_mov_b64_e32 v[66:67], 0
	v_mov_b64_e32 v[68:69], 0
	v_mov_b64_e32 v[70:71], 0
	v_mov_b64_e32 v[72:73], 0
	v_mov_b64_e32 v[74:75], 0
	v_mov_b64_e32 v[76:77], 0
	v_mov_b64_e32 v[78:79], 0
	v_mov_b64_e32 v[80:81], 0
	v_mov_b64_e32 v[82:83], 0
	v_mov_b64_e32 v[84:85], 0
	v_mov_b64_e32 v[86:87], 0
	v_mov_b64_e32 v[88:89], 0
	v_mov_b64_e32 v[90:91], 0
	v_mov_b64_e32 v[92:93], 0
	v_mov_b64_e32 v[94:95], 0
	v_mov_b64_e32 v[96:97], 0
	v_mov_b64_e32 v[98:99], 0
	v_mov_b64_e32 v[100:101], 0
	v_mov_b64_e32 v[102:103], 0
	v_mov_b64_e32 v[104:105], 0
	v_mov_b64_e32 v[106:107], 0
	v_mov_b64_e32 v[108:109], 0
	v_mov_b64_e32 v[110:111], 0
	v_mov_b64_e32 v[112:113], 0
	v_mov_b64_e32 v[114:115], 0
	v_mov_b64_e32 v[116:117], 0
	v_mov_b64_e32 v[118:119], 0
	v_mov_b64_e32 v[120:121], 0
	v_mov_b64_e32 v[122:123], 0
	v_mov_b64_e32 v[124:125], 0
	v_mov_b64_e32 v[126:127], 0
	v_mov_b64_e32 v[128:129], 0
	v_mov_b64_e32 v[130:131], 0
	v_mov_b64_e32 v[132:133], 0
	v_mov_b64_e32 v[134:135], 0
	v_mov_b64_e32 v[136:137], 0
	v_mov_b64_e32 v[138:139], 0
	v_mov_b64_e32 v[140:141], 0
	v_mov_b64_e32 v[142:143], 0
	v_mov_b64_e32 v[144:145], 0
	v_mov_b64_e32 v[146:147], 0
	v_mov_b64_e32 v[148:149], 0
	v_mov_b64_e32 v[150:151], 0
	v_mov_b64_e32 v[152:153], 0
	v_mov_b64_e32 v[154:155], 0
	v_mov_b64_e32 v[156:157], 0
	v_mov_b64_e32 v[158:159], 0
	v_mov_b64_e32 v[160:161], 0
	v_mov_b64_e32 v[162:163], 0
	v_mov_b64_e32 v[164:165], 0
	v_mov_b64_e32 v[166:167], 0
	v_mov_b64_e32 v[168:169], 0
	v_mov_b64_e32 v[170:171], 0
	v_mov_b64_e32 v[172:173], 0
	v_mov_b64_e32 v[174:175], 0
	v_mov_b64_e32 v[176:177], 0
	v_mov_b64_e32 v[178:179], 0
	v_mov_b64_e32 v[180:181], 0
	v_mov_b64_e32 v[182:183], 0
	v_mov_b64_e32 v[184:185], 0
	v_mov_b64_e32 v[186:187], 0
	v_mov_b64_e32 v[188:189], 0
	v_mov_b64_e32 v[190:191], 0
	v_lshl_add_u64 v[204:205], v[0:1], 0, s[30:31]
	v_mov_b32_e32 v211, v193
	s_mov_b32 s25, 0
	s_xor_b64 s[30:31], s[36:37], -1
	s_mov_b64 s[34:35], s[12:13]
	v_mov_b32_e32 v232, v210
	v_mov_b32_e32 v231, v192
	v_mov_b32_e32 v230, v208
	v_mov_b32_e32 v229, v206
	s_branch .LBB0_1183

.LBB0_1262:
	s_mul_i32 s41, s82, 0xe0000
	s_mul_hi_i32 s40, s82, 0xe0000
	s_add_u32 s62, s22, s41
	v_mul_hi_u32 v1, v213, s67
	v_mul_lo_u32 v0, v213, s67
	s_addc_u32 s63, s23, s40
	v_lshl_add_u64 v[0:1], s[14:15], 0, v[0:1]
	s_mul_hi_i32 s41, s81, 0xe0000
	s_mul_i32 s40, s81, 0xe0000
	v_mov_b64_e32 v[32:33], 0
	v_mov_b64_e32 v[34:35], 0
	v_mov_b64_e32 v[36:37], 0
	v_mov_b64_e32 v[38:39], 0
	v_mov_b64_e32 v[40:41], 0
	v_mov_b64_e32 v[42:43], 0
	v_mov_b64_e32 v[44:45], 0
	v_mov_b64_e32 v[46:47], 0
	v_mov_b64_e32 v[48:49], 0
	v_mov_b64_e32 v[50:51], 0
	v_mov_b64_e32 v[52:53], 0
	v_mov_b64_e32 v[54:55], 0
	v_mov_b64_e32 v[56:57], 0
	v_mov_b64_e32 v[58:59], 0
	v_mov_b64_e32 v[60:61], 0
	v_mov_b64_e32 v[62:63], 0
	v_mov_b64_e32 v[64:65], 0
	v_mov_b64_e32 v[66:67], 0
	v_mov_b64_e32 v[68:69], 0
	v_mov_b64_e32 v[70:71], 0
	v_mov_b64_e32 v[72:73], 0
	v_mov_b64_e32 v[74:75], 0
	v_mov_b64_e32 v[76:77], 0
	v_mov_b64_e32 v[78:79], 0
	v_mov_b64_e32 v[80:81], 0
	v_mov_b64_e32 v[82:83], 0
	v_mov_b64_e32 v[84:85], 0
	v_mov_b64_e32 v[86:87], 0
	v_mov_b64_e32 v[88:89], 0
	v_mov_b64_e32 v[90:91], 0
	v_mov_b64_e32 v[92:93], 0
	v_mov_b64_e32 v[94:95], 0
	v_mov_b64_e32 v[96:97], 0
	v_mov_b64_e32 v[98:99], 0
	v_mov_b64_e32 v[100:101], 0
	v_mov_b64_e32 v[102:103], 0
	v_mov_b64_e32 v[104:105], 0
	v_mov_b64_e32 v[106:107], 0
	v_mov_b64_e32 v[108:109], 0
	v_mov_b64_e32 v[110:111], 0
	v_mov_b64_e32 v[112:113], 0
	v_mov_b64_e32 v[114:115], 0
	v_mov_b64_e32 v[116:117], 0
	v_mov_b64_e32 v[118:119], 0
	v_mov_b64_e32 v[120:121], 0
	v_mov_b64_e32 v[122:123], 0
	v_mov_b64_e32 v[124:125], 0
	v_mov_b64_e32 v[126:127], 0
	v_mov_b64_e32 v[128:129], 0
	v_mov_b64_e32 v[130:131], 0
	v_mov_b64_e32 v[132:133], 0
	v_mov_b64_e32 v[134:135], 0
	v_mov_b64_e32 v[136:137], 0
	v_mov_b64_e32 v[138:139], 0
	v_mov_b64_e32 v[140:141], 0
	v_mov_b64_e32 v[142:143], 0
	v_mov_b64_e32 v[144:145], 0
	v_mov_b64_e32 v[146:147], 0
	v_mov_b64_e32 v[148:149], 0
	v_mov_b64_e32 v[150:151], 0
	v_mov_b64_e32 v[152:153], 0
	v_mov_b64_e32 v[154:155], 0
	v_mov_b64_e32 v[156:157], 0
	v_mov_b64_e32 v[158:159], 0
	v_lshl_add_u64 v[208:209], v[0:1], 0, s[40:41]
	v_lshl_add_u64 v[162:163], s[38:39], 0, v[202:203]
	v_lshl_add_u64 v[164:165], s[38:39], 0, v[204:205]
	s_mov_b32 s43, 0

.LBB0_1291:
	v_mul_hi_u32 v1, v184, s6
	v_mul_lo_u32 v0, v184, s6
	s_ashr_i32 s31, s30, 31
	v_lshl_add_u64 v[0:1], s[10:11], 0, v[0:1]
	s_lshl_b64 s[40:41], s[30:31], 18
	v_mov_b64_e32 v[32:33], 0
	v_mov_b64_e32 v[34:35], 0
	v_mov_b64_e32 v[36:37], 0
	v_mov_b64_e32 v[38:39], 0
	v_mov_b64_e32 v[40:41], 0
	v_mov_b64_e32 v[42:43], 0
	v_mov_b64_e32 v[44:45], 0
	v_mov_b64_e32 v[46:47], 0
	v_mov_b64_e32 v[48:49], 0
	v_mov_b64_e32 v[50:51], 0
	v_mov_b64_e32 v[52:53], 0
	v_mov_b64_e32 v[54:55], 0
	v_mov_b64_e32 v[56:57], 0
	v_mov_b64_e32 v[58:59], 0
	v_mov_b64_e32 v[60:61], 0
	v_mov_b64_e32 v[62:63], 0
	v_mov_b64_e32 v[64:65], 0
	v_mov_b64_e32 v[66:67], 0
	v_mov_b64_e32 v[68:69], 0
	v_mov_b64_e32 v[70:71], 0
	v_mov_b64_e32 v[72:73], 0
	v_mov_b64_e32 v[74:75], 0
	v_mov_b64_e32 v[76:77], 0
	v_mov_b64_e32 v[78:79], 0
	v_mov_b64_e32 v[80:81], 0
	v_mov_b64_e32 v[82:83], 0
	v_mov_b64_e32 v[84:85], 0
	v_mov_b64_e32 v[86:87], 0
	v_mov_b64_e32 v[88:89], 0
	v_mov_b64_e32 v[90:91], 0
	v_mov_b64_e32 v[92:93], 0
	v_mov_b64_e32 v[94:95], 0
	v_mov_b64_e32 v[96:97], 0
	v_mov_b64_e32 v[98:99], 0
	v_mov_b64_e32 v[100:101], 0
	v_mov_b64_e32 v[102:103], 0
	v_mov_b64_e32 v[104:105], 0
	v_mov_b64_e32 v[106:107], 0
	v_mov_b64_e32 v[108:109], 0
	v_mov_b64_e32 v[110:111], 0
	v_mov_b64_e32 v[112:113], 0
	v_mov_b64_e32 v[114:115], 0
	v_mov_b64_e32 v[116:117], 0
	v_mov_b64_e32 v[118:119], 0
	v_mov_b64_e32 v[120:121], 0
	v_mov_b64_e32 v[122:123], 0
	v_mov_b64_e32 v[124:125], 0
	v_mov_b64_e32 v[126:127], 0
	v_mov_b64_e32 v[128:129], 0
	v_mov_b64_e32 v[130:131], 0
	v_mov_b64_e32 v[132:133], 0
	v_mov_b64_e32 v[134:135], 0
	v_mov_b64_e32 v[136:137], 0
	v_mov_b64_e32 v[138:139], 0
	v_mov_b64_e32 v[140:141], 0
	v_mov_b64_e32 v[142:143], 0
	v_mov_b64_e32 v[144:145], 0
	v_mov_b64_e32 v[146:147], 0
	v_mov_b64_e32 v[148:149], 0
	v_mov_b64_e32 v[150:151], 0
	v_mov_b64_e32 v[152:153], 0
	v_mov_b64_e32 v[154:155], 0
	v_mov_b64_e32 v[156:157], 0
	v_mov_b64_e32 v[158:159], 0
	v_lshl_add_u64 v[172:173], v[0:1], 0, s[40:41]
	v_mov_b32_e32 v179, v161
	s_mov_b32 s31, 0
	s_xor_b64 s[40:41], s[36:37], -1
	s_mov_b64 s[42:43], s[12:13]
	v_mov_b32_e32 v195, v178
	v_mov_b32_e32 v194, v160
	v_mov_b32_e32 v193, v176
	v_mov_b32_e32 v192, v174
	s_branch .LBB0_1293

.LBB0_1372:
	v_cmp_lt_i64_e64 s[36:37], s[26:27], v[198:199]
	s_mul_i32 s26, s81, 0xe0000
	v_mul_hi_u32 v1, v205, s69
	v_mul_lo_u32 v0, v205, s69
	s_mul_hi_i32 s27, s81, 0xe0000
	s_add_u32 s26, s66, s26
	v_lshl_add_u64 v[0:1], s[14:15], 0, v[0:1]
	s_mul_hi_i32 s31, s80, 0xe0000
	s_mul_i32 s30, s80, 0xe0000
	v_mov_b64_e32 v[32:33], 0
	v_mov_b64_e32 v[34:35], 0
	v_mov_b64_e32 v[36:37], 0
	v_mov_b64_e32 v[38:39], 0
	v_mov_b64_e32 v[40:41], 0
	v_mov_b64_e32 v[42:43], 0
	v_mov_b64_e32 v[44:45], 0
	v_mov_b64_e32 v[46:47], 0
	v_mov_b64_e32 v[48:49], 0
	v_mov_b64_e32 v[50:51], 0
	v_mov_b64_e32 v[52:53], 0
	v_mov_b64_e32 v[54:55], 0
	v_mov_b64_e32 v[56:57], 0
	v_mov_b64_e32 v[58:59], 0
	v_mov_b64_e32 v[60:61], 0
	v_mov_b64_e32 v[62:63], 0
	v_mov_b64_e32 v[64:65], 0
	v_mov_b64_e32 v[66:67], 0
	v_mov_b64_e32 v[68:69], 0
	v_mov_b64_e32 v[70:71], 0
	v_mov_b64_e32 v[72:73], 0
	v_mov_b64_e32 v[74:75], 0
	v_mov_b64_e32 v[76:77], 0
	v_mov_b64_e32 v[78:79], 0
	v_mov_b64_e32 v[80:81], 0
	v_mov_b64_e32 v[82:83], 0
	v_mov_b64_e32 v[84:85], 0
	v_mov_b64_e32 v[86:87], 0
	v_mov_b64_e32 v[88:89], 0
	v_mov_b64_e32 v[90:91], 0
	v_mov_b64_e32 v[92:93], 0
	v_mov_b64_e32 v[94:95], 0
	v_mov_b64_e32 v[96:97], 0
	v_mov_b64_e32 v[98:99], 0
	v_mov_b64_e32 v[100:101], 0
	v_mov_b64_e32 v[102:103], 0
	v_mov_b64_e32 v[104:105], 0
	v_mov_b64_e32 v[106:107], 0
	v_mov_b64_e32 v[108:109], 0
	v_mov_b64_e32 v[110:111], 0
	v_mov_b64_e32 v[112:113], 0
	v_mov_b64_e32 v[114:115], 0
	v_mov_b64_e32 v[116:117], 0
	v_mov_b64_e32 v[118:119], 0
	v_mov_b64_e32 v[120:121], 0
	v_mov_b64_e32 v[122:123], 0
	v_mov_b64_e32 v[124:125], 0
	v_mov_b64_e32 v[126:127], 0
	v_mov_b64_e32 v[128:129], 0
	v_mov_b64_e32 v[130:131], 0
	v_mov_b64_e32 v[132:133], 0
	v_mov_b64_e32 v[134:135], 0
	v_mov_b64_e32 v[136:137], 0
	v_mov_b64_e32 v[138:139], 0
	v_mov_b64_e32 v[140:141], 0
	v_mov_b64_e32 v[142:143], 0
	v_mov_b64_e32 v[144:145], 0
	v_mov_b64_e32 v[146:147], 0
	v_mov_b64_e32 v[148:149], 0
	v_mov_b64_e32 v[150:151], 0
	v_mov_b64_e32 v[152:153], 0
	v_mov_b64_e32 v[154:155], 0
	v_mov_b64_e32 v[156:157], 0
	v_mov_b64_e32 v[158:159], 0
	s_addc_u32 s27, s67, s27
	v_lshl_add_u64 v[200:201], v[0:1], 0, s[30:31]
	v_lshl_add_u64 v[162:163], s[28:29], 0, v[194:195]
	v_lshl_add_u64 v[164:165], s[28:29], 0, v[196:197]
	s_mov_b32 s39, 0
